# attention PV: eight V^T fragment reads in flight AND conflict-free 128-bit reads (key-permuted V^T LDS tile), on top of mask skip and in-register reductions
# speedup vs baseline: 1.0059x; 1.0059x over previous
; __device__ __forceinline__ void phase_attention(const Frame& F, const Args& a) {
;     ...
;     const int fr = F.lane & 15, fq = F.lane >> 4;
;     const int key0 = F.tid >> 4, c16 = F.tid & 15, dim0 = F.tid >> 3, c8 = F.tid & 7;
;     for (int unit = ((F.G % 8 == 0) ? (F.bid % 8) * (F.G / 8) + F.bid / 8 : F.bid); unit < 256; unit += F.G) {
;         const int b = unit >> 7, h = (unit >> 5) & 3, n = unit & 31;
;         const int kt_lo = (2 * n - 2) < 0 ? 0 : (2 * n - 2), kt_hi = (2 * n + 3) > 63 ? 63 : (2 * n + 3), nband = kt_hi - kt_lo + 1, ntile = nband + 4, nstep = 2 * ntile;
;         u32x4 kreg[2], vreg[2];
;         const bf16_t* kbase = QK + 2048 + h * 128 + 8 * c16; const bf16_t* vbase = VT + (size_t)(h * 128 + dim0) * T0 + 8 * c8;
.LBB0_2767:
	s_cmp_lt_i32 s94, 14
	s_cselect_b64 s[0:1], -1, 0
	s_and_b64 s[4:5], s[0:1], s[4:5]
	s_andn2_b64 vcc, exec, s[4:5]
	s_cbranch_vccnz .LBB0_2792
	v_readlane_b32 s0, v254, 0
	v_readlane_b32 s1, v254, 1
	s_mov_b32 s2, s0
	s_ashr_i32 s1, s2, 3
	s_ashr_i32 s2, s3, 31
	s_lshr_b32 s2, s2, 29
	s_add_i32 s2, s3, s2
	s_and_b32 s6, s2, -8
	s_sub_i32 s6, s3, s6
	s_mul_i32 s1, s1, s6
	s_ashr_i32 s2, s2, 3
	s_and_b32 s0, s0, 7
	s_add_i32 s1, s1, s2
	s_cmp_eq_u32 s0, 0
	s_cselect_b32 s18, s1, s3
	s_cmpk_gt_i32 s18, 0xff
	s_mov_b32 s7, 0
	s_cbranch_scc1 .LBB0_2792
	v_lshlrev_b32_e32 v6, 3, v0
	v_and_b32_e32 v2, 0x78, v6
	v_lshlrev_b32_e32 v150, 1, v2
	v_mov_b32_e32 v2, 0
	v_mov_b32_e32 v151, v2
	v_lshl_add_u64 v[4:5], s[92:93], 0, v[150:151]
	s_mov_b64 s[0:1], 0x3a601000
	v_lshl_add_u64 v[152:153], v[4:5], 0, s[0:1]
	v_and_b32_e32 v4, 56, v6
	v_lshlrev_b32_e32 v154, 1, v4
	v_mov_b32_e32 v155, v2
	v_lshl_add_u64 v[4:5], s[92:93], 0, v[154:155]
	s_mov_b64 s[0:1], 0x3d900000
	v_lshl_add_u64 v[156:157], v[4:5], 0, s[0:1]
	v_and_b32_e32 v4, 48, v1
	v_mov_b32_e32 v5, v2
	v_lshrrev_b32_e32 v3, 4, v1
	v_lshl_add_u64 v[4:5], s[92:93], 0, v[4:5]
	s_mov_b64 s[0:1], 0x3a600000
	v_lshl_add_u64 v[158:159], v[4:5], 0, s[0:1]
	v_lshlrev_b32_e32 v4, 2, v3
	v_mov_b32_e32 v5, v2
	v_and_b32_e32 v172, 15, v0
	v_lshrrev_b32_e32 v173, 4, v0
	v_lshrrev_b32_e32 v174, 3, v0
	v_lshl_add_u64 v[6:7], s[92:93], 0, v[4:5]
	s_mov_b64 s[0:1], 0x41b00000
	v_mul_u32_u24_e32 v8, 0x88, v173
	v_mul_u32_u24_e32 v9, 0x48, v174
	v_lshlrev_b32_e32 v151, 4, v3
	v_lshl_add_u64 v[160:161], v[6:7], 0, s[0:1]
	v_sub_u32_e32 v3, v4, v172
	v_readlane_b32 s0, v254, 2
	v_lshlrev_b32_e32 v177, 1, v8
	v_lshlrev_b32_e32 v179, 1, v9
	v_add_u32_e32 v181, 0xffffff7f, v3
	s_lshr_b32 s19, s0, 8
	s_lshl_b32 s0, s74, 5
	v_mbcnt_lo_u32_b32 v3, -1, 0
	v_and_b32_e32 v155, 48, v0
	v_mul_u32_u24_e32 v175, 0x110, v172
	v_mul_u32_u24_e32 v176, 0x90, v172
	v_add3_u32 v178, 0, v177, v150
	v_add3_u32 v180, 0, v179, v154
	v_and_b32_e32 v249, 4, v0
	v_lshlrev_b32_e32 v249, 4, v249
	v_and_b32_e32 v252, 1, v0
	v_lshl_or_b32 v249, v252, 5, v249
	v_and_b32_e32 v252, 2, v0
	v_lshl_or_b32 v249, v252, 2, v249
	s_and_b32 s20, s0, 0x60
	s_movk_i32 s21, 0x1400
	s_mov_b64 s[8:9], 0x110000
	s_movk_i32 s22, 0xfeff
	s_mov_b32 s23, 0xff800000
	s_movk_i32 s24, 0xfefe
	s_mov_b32 s25, 0x41800000
	s_mov_b32 s26, 0xc3e00000
	v_mbcnt_hi_u32_b32 v182, -1, v3
	v_mov_b32_e32 v183, 0xff800000
	v_mov_b32_e32 v184, 0x43e00000
	s_branch .LBB0_2772

; __device__ __forceinline__ void phase_attention(const Frame& F, const Args& a) {
;     ...
;         const int b = unit >> 7, h = (unit >> 5) & 3, n = unit & 31;
;         const int kt_lo = (2 * n - 2) < 0 ? 0 : (2 * n - 2), kt_hi = (2 * n + 3) > 63 ? 63 : (2 * n + 3), nband = kt_hi - kt_lo + 1, ntile = nband + 4, nstep = 2 * ntile;
;         u32x4 kreg[2], vreg[2];
;         const bf16_t* kbase = QK + 2048 + h * 128 + 8 * c16; const bf16_t* vbase = VT + (size_t)(h * 128 + dim0) * T0 + 8 * c8;
;     ...
;         __syncthreads();
;         ATT_LOAD(0); ATT_STORE(0);
;         __syncthreads();
;         bf16x8 aq[2][4]; float mrun[2], lrun[2]; f32x4 o[2][8]; int qh = 0, qpos0 = 0, qrow = 0;
.LBB0_2776:
	s_bfe_u32 s10, s18, 0x20005
	s_lshl_b32 s1, s10, 7
	v_or_b32_e32 v3, s1, v174
	v_mul_u32_u24_e32 v66, 0x4400, v3
	s_lshl_b32 s6, s1, 1
	v_mov_b32_e32 v67, v2
	v_lshl_add_u64 v[162:163], v[152:153], 0, s[6:7]
	v_lshl_add_u64 v[164:165], v[156:157], 0, v[66:67]
	v_add_u32_e32 v3, s0, v173
	s_ashr_i32 s1, s0, 31
	v_mad_i64_i32 v[66:67], s[16:17], v3, s21, v[162:163]
	v_add_u32_e32 v3, 32, v3
	s_lshl_b64 s[0:1], s[0:1], 1
	v_lshl_add_u64 v[166:167], v[164:165], 0, s[8:9]
	v_mad_i64_i32 v[74:75], s[16:17], v3, s21, v[162:163]
	v_lshl_add_u64 v[78:79], v[164:165], 0, s[0:1]
	v_lshl_add_u64 v[82:83], v[166:167], 0, s[0:1]
	global_load_dwordx4 v[66:69], v[66:67], off
	s_nop 0
	global_load_dwordx4 v[74:77], v[74:75], off
	s_nop 0
	global_load_dwordx4 v[78:81], v[78:79], off
	s_nop 0
	global_load_dwordx4 v[82:85], v[82:83], off
	s_cmp_lt_i32 s27, -4
	s_waitcnt vmcnt(3)
	ds_write_b128 v178, v[66:69]
	s_waitcnt vmcnt(2)
	ds_write_b128 v178, v[74:77] offset:8704
	s_waitcnt vmcnt(1)
	v_add_u32_e32 v252, v179, v249
	v_add_u32_e32 v250, 0x4400, v252
	v_add_u32_e32 v251, 0x6800, v252
	ds_write2_b64 v250, v[78:79], v[80:81] offset1:2
	s_waitcnt vmcnt(0)
	ds_write2_b64 v251, v[82:83], v[84:85] offset1:2
	s_waitcnt lgkmcnt(0)
	s_barrier
	s_cbranch_scc1 .LBB0_2771
	v_and_b32_e32 v5, 64, v182
	v_xor_b32_e32 v3, 16, v182
	v_add_u32_e32 v5, 64, v5
	v_cmp_lt_i32_e32 vcc, v3, v5
	s_add_i32 s11, s27, 5
	s_sub_i32 s33, -5, s27
	v_cndmask_b32_e32 v3, v182, v3, vcc
	v_lshlrev_b32_e32 v185, 2, v3
	v_xor_b32_e32 v3, 32, v182
	v_cmp_lt_i32_e32 vcc, v3, v5
	s_max_i32 s34, s11, s33
	s_lshl_b32 s29, s14, 12
	v_cndmask_b32_e32 v3, v182, v3, vcc
	v_lshlrev_b32_e32 v186, 2, v3
	v_cvt_f32_u32_e32 v3, s34
	s_lshl_b32 s0, s13, 7
	s_bitset1_b32 s29, 9
	s_or_b32 s35, s0, s20
	v_rcp_iflag_f32_e32 v3, v3
	s_add_i32 s36, s29, s35
	v_or_b32_e32 v5, s36, v172
	v_mad_i64_i32 v[168:169], s[0:1], v5, s21, 0
	v_mul_f32_e32 v3, 0x4f7ffffe, v3
	v_cvt_u32_f32_e32 v3, v3
	v_or_b32_e32 v5, 16, v5
	v_mad_i64_i32 v[170:171], s[0:1], v5, s21, 0
	s_sub_i32 s0, 0, s34
	v_readfirstlane_b32 s1, v3
	s_mul_i32 s0, s0, s1
	s_lshl_b32 s31, s10, 2
	s_mul_hi_u32 s0, s1, s0
	s_sub_i32 s39, s2, s12
	s_lshl_b32 s6, s11, 1
	s_lshl_b32 s30, s14, 8
	s_mov_b32 s10, 0
	s_add_i32 s31, s31, s19
	s_ashr_i32 s37, s11, 31
	s_add_i32 s38, s1, s0
	s_add_i32 s39, s39, -4
	s_mov_b32 s41, 0
	s_mov_b32 s11, 0
	s_mov_b32 s42, 0

; __device__ __forceinline__ void phase_attention(const Frame& F, const Args& a) {
;     ...
;                 float mx = s[m][0][0];
; #pragma unroll
;                 for (int nn = 0; nn < 4; ++nn)
; #pragma unroll
;                     for (int j = 0; j < 4; ++j) mx = fmaxf(mx, s[m][nn][j]);
;                 mx = fmaxf(mx, __shfl_xor(mx, 16)); mx = fmaxf(mx, __shfl_xor(mx, 32));
;                 const float mnew = fmaxf(mrun[m], mx), alpha = __expf(mrun[m] - mnew); mrun[m] = mnew;
;                 float rs = 0.f;
; #pragma unroll
;                 for (int nn = 0; nn < 4; ++nn)
; #pragma unroll
;                     for (int j = 0; j < 4; ++j) { const float p = __expf(s[m][nn][j] - mnew); s[m][nn][j] = p; rs += p; }
;                 rs += __shfl_xor(rs, 16); rs += __shfl_xor(rs, 32);
;                 lrun[m] = lrun[m] * alpha + rs;
; #pragma unroll
;                 for (int nd = 0; nd < 8; ++nd) o[m][nd] = o[m][nd] * alpha;
.LBB0_2786:
	s_waitcnt lgkmcnt(0)
	v_add_f32_e32 v5, v142, v143
	v_max_f32_e32 v142, v139, v139
	v_max_f32_e32 v143, v138, v138
	v_max_f32_e32 v142, v143, v142
	v_max3_f32 v142, v142, v140, v141
	v_max3_f32 v142, v142, v134, v135
	v_max3_f32 v142, v142, v136, v137
	v_max3_f32 v142, v142, v130, v131
	v_max3_f32 v142, v142, v132, v133
	v_max3_f32 v142, v142, v122, v123
	v_max3_f32 v142, v142, v124, v125
	v_mov_b32_e32 v143, v142
	s_nop 1
	v_permlane16_swap_b32 v143, v142
	v_sub_f32_e32 v4, v4, v3
	v_mul_f32_e32 v4, 0x3fb8aa3b, v4
	v_exp_f32_e32 v4, v4
	s_add_i32 s0, s39, s42
	s_waitcnt lgkmcnt(0)
	v_max_f32_e32 v143, v143, v143
	v_max_f32_e32 v142, v142, v143
	v_mov_b32_e32 v143, v142
	s_nop 1
	v_permlane32_swap_b32 v143, v142
	v_fmac_f32_e32 v5, v189, v4
	v_pk_mul_f32 v[116:117], v[116:117], v[4:5] op_sel_hi:[1,0]
	v_pk_mul_f32 v[114:115], v[114:115], v[4:5] op_sel_hi:[1,0]
	v_pk_mul_f32 v[112:113], v[112:113], v[4:5] op_sel_hi:[1,0]
	s_waitcnt lgkmcnt(0)
	v_max3_f32 v142, v187, v142, v143
	v_sub_f32_e32 v138, v138, v142
	v_mul_f32_e32 v138, 0x3fb8aa3b, v138
	v_sub_f32_e32 v139, v139, v142
	v_exp_f32_e32 v138, v138
	v_mul_f32_e32 v139, 0x3fb8aa3b, v139
	v_sub_f32_e32 v140, v140, v142
	v_exp_f32_e32 v139, v139
	v_mul_f32_e32 v140, 0x3fb8aa3b, v140
	v_sub_f32_e32 v141, v141, v142
	v_exp_f32_e32 v140, v140
	v_mul_f32_e32 v141, 0x3fb8aa3b, v141
	v_sub_f32_e32 v134, v134, v142
	v_exp_f32_e32 v141, v141
	v_mul_f32_e32 v134, 0x3fb8aa3b, v134
	v_sub_f32_e32 v135, v135, v142
	v_add_f32_e32 v143, 0, v138
	v_exp_f32_e32 v134, v134
	v_mul_f32_e32 v135, 0x3fb8aa3b, v135
	v_sub_f32_e32 v136, v136, v142
	v_sub_f32_e32 v130, v130, v142
	v_add_f32_e32 v143, v139, v143
	v_exp_f32_e32 v135, v135
	v_mul_f32_e32 v136, 0x3fb8aa3b, v136
	v_sub_f32_e32 v137, v137, v142
	v_mul_f32_e32 v130, 0x3fb8aa3b, v130
	v_add_f32_e32 v143, v140, v143
	v_exp_f32_e32 v136, v136
	v_mul_f32_e32 v137, 0x3fb8aa3b, v137
	v_exp_f32_e32 v144, v130
	v_sub_f32_e32 v130, v131, v142
	v_add_f32_e32 v143, v141, v143
	v_exp_f32_e32 v137, v137
	v_mul_f32_e32 v130, 0x3fb8aa3b, v130
	v_add_f32_e32 v143, v134, v143
	v_exp_f32_e32 v145, v130
	v_sub_f32_e32 v130, v132, v142
	v_add_f32_e32 v143, v135, v143
	v_mul_f32_e32 v130, 0x3fb8aa3b, v130
	v_add_f32_e32 v143, v136, v143
	v_exp_f32_e32 v146, v130
	v_sub_f32_e32 v130, v133, v142
	v_sub_f32_e32 v122, v122, v142
	v_add_f32_e32 v143, v137, v143
	v_mul_f32_e32 v130, 0x3fb8aa3b, v130
	v_mul_f32_e32 v122, 0x3fb8aa3b, v122
	v_exp_f32_e32 v147, v130
	v_add_f32_e32 v130, v144, v143
	v_exp_f32_e32 v143, v122
	v_sub_f32_e32 v122, v123, v142
	v_mul_f32_e32 v122, 0x3fb8aa3b, v122
	v_exp_f32_e32 v123, v122
	v_sub_f32_e32 v122, v124, v142
	v_mul_f32_e32 v122, 0x3fb8aa3b, v122
	v_add_f32_e32 v130, v145, v130
	v_exp_f32_e32 v124, v122
	v_sub_f32_e32 v122, v125, v142
	v_add_f32_e32 v130, v146, v130
	v_mul_f32_e32 v122, 0x3fb8aa3b, v122
	v_add_f32_e32 v130, v147, v130
	v_exp_f32_e32 v125, v122
	v_add_f32_e32 v122, v143, v130
	v_add_f32_e32 v122, v123, v122
	v_add_f32_e32 v122, v124, v122
	v_add_f32_e32 v122, v125, v122
	v_mov_b32_e32 v130, v122
	s_nop 1
	v_permlane16_swap_b32 v130, v122
	v_pk_mul_f32 v[110:111], v[110:111], v[4:5] op_sel_hi:[1,0]
	v_pk_mul_f32 v[96:97], v[96:97], v[4:5] op_sel_hi:[1,0]
	v_pk_mul_f32 v[94:95], v[94:95], v[4:5] op_sel_hi:[1,0]
	v_pk_mul_f32 v[100:101], v[100:101], v[4:5] op_sel_hi:[1,0]
	s_waitcnt lgkmcnt(0)
	v_add_f32_e32 v122, v122, v130
	v_pk_mul_f32 v[98:99], v[98:99], v[4:5] op_sel_hi:[1,0]
	v_pk_mul_f32 v[104:105], v[104:105], v[4:5] op_sel_hi:[1,0]
	v_pk_mul_f32 v[102:103], v[102:103], v[4:5] op_sel_hi:[1,0]
	v_pk_mul_f32 v[108:109], v[108:109], v[4:5] op_sel_hi:[1,0]
	v_pk_mul_f32 v[106:107], v[106:107], v[4:5] op_sel_hi:[1,0]
	v_pk_mul_f32 v[88:89], v[88:89], v[4:5] op_sel_hi:[1,0]
	v_pk_mul_f32 v[86:87], v[86:87], v[4:5] op_sel_hi:[1,0]
	v_pk_mul_f32 v[92:93], v[92:93], v[4:5] op_sel_hi:[1,0]
	v_pk_mul_f32 v[90:91], v[90:91], v[4:5] op_sel_hi:[1,0]
	v_sub_f32_e32 v4, v187, v142
	v_mov_b32_e32 v130, v122
	s_nop 1
	v_permlane32_swap_b32 v130, v122
	v_mul_f32_e32 v4, 0x3fb8aa3b, v4
	v_exp_f32_e32 v4, v4
	s_add_i32 s0, s0, s43
	s_waitcnt lgkmcnt(0)
; #define LAS __attribute__((address_space(3)))
; __device__ __forceinline__ unsigned cvt_pk_bf16(float lo, float hi) { unsigned r; asm volatile("v_cvt_pk_bf16_f32 %0, %1, %2" : "=v"(r) : "v"(lo), "v"(hi)); return r; }
; __device__ __forceinline__ void phase_attention(const Frame& F, const Args& a) {
;     ...
;                 for (int ks = 0; ks < 2; ++ks) { u32x4 w; w.x = cvt_pk_bf16(s[m][2 * ks][0], s[m][2 * ks][1]); w.y = cvt_pk_bf16(s[m][2 * ks][2], s[m][2 * ks][3]);
;                     w.z = cvt_pk_bf16(s[m][2 * ks + 1][0], s[m][2 * ks + 1][1]); w.w = cvt_pk_bf16(s[m][2 * ks + 1][2], s[m][2 * ks + 1][3]); pf[m][ks] = __builtin_bit_cast(bf16x8, w); }
;             }
;             __builtin_amdgcn_s_setprio(1);
; #pragma unroll
;             for (int ks = 0; ks < 2; ++ks)
; #pragma unroll
;                 for (int nd = 0; nd < 8; ++nd) { const LAS bf16_t* vp = Vs + (16 * nd + fr) * 72 + 32 * ks + 4 * fq;
;                     u32x4 w; const u32x2 lo = *(const LAS u32x2*)vp, hi = *(const LAS u32x2*)(vp + 16); w.x = lo.x; w.y = lo.y; w.z = hi.x; w.w = hi.y;
;                     const bf16x8 vf = __builtin_bit_cast(bf16x8, w);
; #pragma unroll
;                     for (int m = 0; m < 2; ++m) o[m][nd] = __builtin_amdgcn_mfma_f32_16x16x32_bf16(vf, pf[m][ks], o[m][nd], 0, 0, 0); }
;     ...
;             if (step + 1 < nstep) ATT_STORE((step + 1) & 1);
	v_add_f32_e32 v122, v122, v130
	v_fmac_f32_e32 v122, v188, v4
	v_pk_mul_f32 v[72:73], v[72:73], v[4:5] op_sel_hi:[1,0]
	v_pk_mul_f32 v[70:71], v[70:71], v[4:5] op_sel_hi:[1,0]
	v_pk_mul_f32 v[64:65], v[64:65], v[4:5] op_sel_hi:[1,0]
	v_pk_mul_f32 v[62:63], v[62:63], v[4:5] op_sel_hi:[1,0]
	v_pk_mul_f32 v[60:61], v[60:61], v[4:5] op_sel_hi:[1,0]
	v_pk_mul_f32 v[58:59], v[58:59], v[4:5] op_sel_hi:[1,0]
	v_pk_mul_f32 v[56:57], v[56:57], v[4:5] op_sel_hi:[1,0]
	v_pk_mul_f32 v[54:55], v[54:55], v[4:5] op_sel_hi:[1,0]
	v_pk_mul_f32 v[52:53], v[52:53], v[4:5] op_sel_hi:[1,0]
	v_pk_mul_f32 v[50:51], v[50:51], v[4:5] op_sel_hi:[1,0]
	v_pk_mul_f32 v[48:49], v[48:49], v[4:5] op_sel_hi:[1,0]
	v_pk_mul_f32 v[46:47], v[46:47], v[4:5] op_sel_hi:[1,0]
	v_pk_mul_f32 v[44:45], v[44:45], v[4:5] op_sel_hi:[1,0]
	v_pk_mul_f32 v[42:43], v[42:43], v[4:5] op_sel_hi:[1,0]
	v_pk_mul_f32 v[40:41], v[40:41], v[4:5] op_sel_hi:[1,0]
	v_pk_mul_f32 v[38:39], v[38:39], v[4:5] op_sel_hi:[1,0]
	v_cvt_pk_bf16_f32 v130, v138, v139
	v_cvt_pk_bf16_f32 v131, v140, v141
	v_cvt_pk_bf16_f32 v132, v134, v135
	v_cvt_pk_bf16_f32 v133, v136, v137
	v_cvt_pk_bf16_f32 v134, v144, v145
	v_cvt_pk_bf16_f32 v135, v146, v147
	v_cvt_pk_bf16_f32 v136, v143, v123
	v_cvt_pk_bf16_f32 v137, v124, v125
	s_setprio 1
	v_add3_u32 v4, s44, v151, v176
	v_add_u32_e32 v123, 0x4000, v4
	v_add_u32_e32 v143, 0x4800, v4
	v_add_u32_e32 v144, 0x5000, v4
	v_add_u32_e32 v145, 0x5800, v4
	v_add_u32_e32 v146, 0x6800, v4
	v_add_u32_e32 v147, 0x7000, v4
	v_add_u32_e32 v148, 0x7800, v4
	v_add_u32_e32 v4, 0x8000, v4
	ds_read_b128 v[138:141], v123 offset:1024
	ds_read_b128 v[224:227], v143 offset:1280
	ds_read_b128 v[228:231], v144 offset:1536
	ds_read_b128 v[232:235], v145 offset:1792
	ds_read_b128 v[236:239], v146
	ds_read_b128 v[240:243], v147 offset:256
	ds_read_b128 v[244:247], v148 offset:512
	ds_read_b128 v[250:253], v4 offset:768
	s_waitcnt lgkmcnt(7)
	v_mfma_f32_16x16x32_bf16 v[114:117], v[138:141], v[126:129], v[114:117]
	v_mfma_f32_16x16x32_bf16 v[70:73], v[138:141], v[130:133], v[70:73]
	ds_read_b128 v[138:141], v123 offset:1088
	s_waitcnt lgkmcnt(7)
	v_mfma_f32_16x16x32_bf16 v[110:113], v[224:227], v[126:129], v[110:113]
	v_mfma_f32_16x16x32_bf16 v[62:65], v[224:227], v[130:133], v[62:65]
	ds_read_b128 v[224:227], v143 offset:1344
	s_waitcnt lgkmcnt(7)
	v_mfma_f32_16x16x32_bf16 v[94:97], v[228:231], v[126:129], v[94:97]
	v_mfma_f32_16x16x32_bf16 v[58:61], v[228:231], v[130:133], v[58:61]
	ds_read_b128 v[228:231], v144 offset:1600
	s_waitcnt lgkmcnt(7)
	v_mfma_f32_16x16x32_bf16 v[98:101], v[232:235], v[126:129], v[98:101]
	v_mfma_f32_16x16x32_bf16 v[54:57], v[232:235], v[130:133], v[54:57]
	ds_read_b128 v[232:235], v145 offset:1856
	s_waitcnt lgkmcnt(7)
	v_mfma_f32_16x16x32_bf16 v[102:105], v[236:239], v[126:129], v[102:105]
	v_mfma_f32_16x16x32_bf16 v[50:53], v[236:239], v[130:133], v[50:53]
	ds_read_b128 v[236:239], v146 offset:64
	s_waitcnt lgkmcnt(7)
	v_mfma_f32_16x16x32_bf16 v[106:109], v[240:243], v[126:129], v[106:109]
	v_mfma_f32_16x16x32_bf16 v[46:49], v[240:243], v[130:133], v[46:49]
	ds_read_b128 v[240:243], v147 offset:320
	s_waitcnt lgkmcnt(7)
	v_mfma_f32_16x16x32_bf16 v[86:89], v[244:247], v[126:129], v[86:89]
	v_mfma_f32_16x16x32_bf16 v[42:45], v[244:247], v[130:133], v[42:45]
	ds_read_b128 v[244:247], v148 offset:576
	s_waitcnt lgkmcnt(7)
	v_mfma_f32_16x16x32_bf16 v[90:93], v[250:253], v[126:129], v[90:93]
	v_mfma_f32_16x16x32_bf16 v[38:41], v[250:253], v[130:133], v[38:41]
	ds_read_b128 v[250:253], v4 offset:832
	s_waitcnt lgkmcnt(7)
	v_mfma_f32_16x16x32_bf16 v[114:117], v[138:141], v[118:121], v[114:117]
	v_mfma_f32_16x16x32_bf16 v[70:73], v[138:141], v[134:137], v[70:73]
	s_waitcnt lgkmcnt(6)
	v_mfma_f32_16x16x32_bf16 v[110:113], v[224:227], v[118:121], v[110:113]
	v_mfma_f32_16x16x32_bf16 v[62:65], v[224:227], v[134:137], v[62:65]
	s_waitcnt lgkmcnt(5)
	v_mfma_f32_16x16x32_bf16 v[94:97], v[228:231], v[118:121], v[94:97]
	v_mfma_f32_16x16x32_bf16 v[58:61], v[228:231], v[134:137], v[58:61]
	s_waitcnt lgkmcnt(4)
	v_mfma_f32_16x16x32_bf16 v[98:101], v[232:235], v[118:121], v[98:101]
	v_mfma_f32_16x16x32_bf16 v[54:57], v[232:235], v[134:137], v[54:57]
	s_waitcnt lgkmcnt(3)
	v_mfma_f32_16x16x32_bf16 v[102:105], v[236:239], v[118:121], v[102:105]
	v_mfma_f32_16x16x32_bf16 v[50:53], v[236:239], v[134:137], v[50:53]
	s_waitcnt lgkmcnt(2)
	v_mfma_f32_16x16x32_bf16 v[106:109], v[240:243], v[118:121], v[106:109]
	v_mfma_f32_16x16x32_bf16 v[46:49], v[240:243], v[134:137], v[46:49]
	s_waitcnt lgkmcnt(1)
	v_mfma_f32_16x16x32_bf16 v[86:89], v[244:247], v[118:121], v[86:89]
	v_mfma_f32_16x16x32_bf16 v[42:45], v[244:247], v[134:137], v[42:45]
	s_waitcnt lgkmcnt(0)
	v_mfma_f32_16x16x32_bf16 v[90:93], v[250:253], v[118:121], v[90:93]
	v_mfma_f32_16x16x32_bf16 v[38:41], v[250:253], v[134:137], v[38:41]
	s_setprio 0
	s_cmp_lg_u32 s0, 0
	s_cbranch_scc0 .LBB0_2791
	s_andn2_b64 vcc, exec, s[14:15]
	s_cbranch_vccnz .LBB0_2789
.LBB0_2788:
	s_bitcmp1_b32 s40, 0
	s_cselect_b32 s0, 0x8c00, 0
	s_add_i32 s0, s0, 0
	v_add3_u32 v4, s0, v177, v150
	ds_write_b128 v4, v[66:69]
	ds_write_b128 v4, v[74:77] offset:8704
	v_add3_u32 v4, s0, v179, v249
	v_add_u32_e32 v250, 0x4400, v4
	v_add_u32_e32 v251, 0x6800, v4
	ds_write2_b64 v250, v[78:79], v[80:81] offset1:2
	ds_write2_b64 v251, v[82:83], v[84:85] offset1:2
